# COMBINE row loops (both layers): next row's routing indices loaded at the top of the current iteration and handed over by v_mov (one memory latency per row instead of two)
# baseline (speedup 1.0000x reference)
.LBB0_1409:
	s_or_b64 exec, exec, s[2:3]
	s_ashr_i32 s12, s12, 6
	s_lshl_b32 s3, s10, 3
	s_lshl_b32 s2, s11, 3
	v_and_b32_e32 v1, 63, v0
	s_add_i32 s4, s3, s12
	s_cmpk_gt_i32 s4, 0x21ff
	v_lshlrev_b32_e32 v2, 2, v1
	v_lshlrev_b32_e32 v3, 4, v1
	s_waitcnt lgkmcnt(0)
	s_barrier
	s_cbranch_scc1 .LBB0_1412
	s_add_u32 s13, s0, 0x326b8000
	s_addc_u32 s16, s1, 0
	s_add_u32 s17, s0, 0x326c9000
	s_addc_u32 s18, s1, 0
	s_add_u32 s19, s0, 0x326da000
	s_addc_u32 s20, s1, 0
	s_add_u32 s21, s0, 0x10000
	s_addc_u32 s22, s1, 0
	v_mov_b32_e32 v5, 0
	v_lshlrev_b32_e32 v4, 3, v1
	s_add_i32 s3, 0, 0x10000
	v_lshl_add_u64 v[6:7], s[0:1], 0, v[4:5]
	s_mov_b64 s[6:7], 0x43d1c000
	v_add_u32_e32 v4, s3, v3
	s_add_i32 s3, 0, 0x16000
	s_ashr_i32 s5, s4, 31
	v_lshl_add_u64 v[6:7], v[6:7], 0, s[6:7]
	v_add_u32_e32 v18, s3, v3
	s_lshl_b64 s[6:7], s[4:5], 11
	s_ashr_i32 s3, s2, 31
	s_lshl_b64 s[8:9], s[4:5], 12
	v_or_b32_e32 v12, 0x400, v2
	v_or_b32_e32 v14, 0x500, v2
	v_or_b32_e32 v16, 0x600, v2
	v_or_b32_e32 v24, 0x700, v2
	v_or_b32_e32 v8, s6, v2
	v_mov_b32_e32 v9, s7
	s_lshl_b64 s[6:7], s[2:3], 11
	v_lshl_or_b32 v10, v1, 3, s8
	v_mov_b32_e32 v11, s9
	s_lshl_b64 s[8:9], s[2:3], 12
	s_lshl_b32 s3, s10, 4
	s_lshl_b32 s5, s12, 1
	s_add_i32 s10, s3, s5
	s_lshl_b32 s3, s11, 4
	s_add_i32 s5, 0, 0x20040
	s_mov_b32 s23, 0x29eb8000
	v_lshlrev_b32_e32 v19, 2, v2
	v_lshlrev_b32_e32 v20, 2, v12
	v_lshlrev_b32_e32 v21, 2, v14
	v_lshlrev_b32_e32 v22, 2, v16
	v_lshlrev_b32_e32 v23, 2, v24
	s_mov_b32 s24, 0x2e2b8000
	v_mov_b32_e32 v24, 0x358637bd
	s_mov_b32 s25, 0x800000
	s_mov_b32 s26, 0x1f4b8000
	s_mov_b32 s27, 0xc3e00000
	v_mov_b32_e32 v25, 0x43e00000
	s_mov_b32 s28, 0x3280c000
	s_mov_b32 s29, s4
	s_mov_b32 s40, s10
	s_ashr_i32 s41, s40, 31
	s_lshl_b64 s[30:31], s[40:41], 2
	s_add_u32 s38, s13, s30
	s_addc_u32 s39, s16, s31
	global_load_dwordx2 v[186:187], v5, s[38:39]
	s_add_u32 s38, s17, s30
	s_addc_u32 s39, s18, s31
	global_load_dword v188, v5, s[38:39]
	s_add_u32 s38, s19, s30
	s_addc_u32 s39, s20, s31
	global_load_dword v190, v5, s[38:39]
	s_add_i32 s40, s40, 1
	s_ashr_i32 s41, s40, 31
	s_lshl_b64 s[30:31], s[40:41], 2
	s_add_u32 s38, s17, s30
	s_addc_u32 s39, s18, s31
	global_load_dword v189, v5, s[38:39]
	s_add_u32 s38, s19, s30
	s_addc_u32 s39, s20, s31
	global_load_dword v191, v5, s[38:39]
	s_waitcnt vmcnt(0)
.LBB0_1411:
	v_mov_b32_e32 v84, v186
	v_mov_b32_e32 v85, v187
	v_mov_b32_e32 v75, v188
	v_mov_b32_e32 v87, v189
	v_mov_b32_e32 v86, v190
	v_mov_b32_e32 v88, v191
	v_lshl_add_u64 v[12:13], s[0:1], 0, v[10:11]
	v_add_co_u32_e32 v34, vcc, s23, v12
	s_add_i32 s40, s10, s3
	s_nop 0
	v_addc_co_u32_e32 v35, vcc, 0, v13, vcc
	s_ashr_i32 s41, s40, 31
	s_lshl_b64 s[30:31], s[40:41], 2
	s_add_u32 s38, s13, s30
	s_addc_u32 s39, s16, s31
	global_load_dwordx2 v[186:187], v5, s[38:39]
	s_add_u32 s38, s17, s30
	s_addc_u32 s39, s18, s31
	global_load_dword v188, v5, s[38:39]
	s_add_u32 s38, s19, s30
	s_addc_u32 s39, s20, s31
	global_load_dword v190, v5, s[38:39]
	s_add_i32 s40, s40, 1
	s_ashr_i32 s41, s40, 31
	s_lshl_b64 s[30:31], s[40:41], 2
	s_add_u32 s38, s17, s30
	s_addc_u32 s39, s18, s31
	global_load_dword v189, v5, s[38:39]
	s_add_u32 s38, s19, s30
	s_addc_u32 s39, s20, s31
	global_load_dword v191, v5, s[38:39]
	global_load_dwordx2 v[66:67], v[34:35], off nt
	global_load_dwordx2 v[68:69], v[34:35], off offset:512 nt
	global_load_dwordx2 v[70:71], v[34:35], off offset:1024 nt
	global_load_dwordx2 v[72:73], v[34:35], off offset:1536 nt
	global_load_dwordx2 v[76:77], v[34:35], off offset:2048 nt
	global_load_dwordx2 v[78:79], v[34:35], off offset:2560 nt
	global_load_dwordx2 v[80:81], v[34:35], off offset:3072 nt
	global_load_dwordx2 v[82:83], v[34:35], off offset:3584 nt
	s_min_i32 s11, s29, 0x2000
	s_ashr_i32 s30, s11, 12
	s_mul_i32 s30, s30, 6
	s_ashr_i32 s31, s30, 31
	s_lshl_b64 s[30:31], s[30:31], 13
	s_add_u32 s30, s21, s30
	s_addc_u32 s31, s22, s31
	s_add_u32 s30, s30, 0xa000
	s_addc_u32 s31, s31, 0
	global_load_dwordx4 v[34:37], v19, s[30:31]
	global_load_dwordx4 v[38:41], v19, s[30:31] offset:1024
	global_load_dwordx4 v[42:45], v19, s[30:31] offset:2048
	global_load_dwordx4 v[46:49], v19, s[30:31] offset:3072
	global_load_dwordx4 v[50:53], v20, s[30:31]
	global_load_dwordx4 v[54:57], v21, s[30:31]
	global_load_dwordx4 v[58:61], v22, s[30:31]
	global_load_dwordx4 v[62:65], v23, s[30:31]
	v_add_co_u32_e32 v16, vcc, s24, v12
	s_lshl_b32 s11, s11, 1
	s_nop 0
	v_addc_co_u32_e32 v17, vcc, 0, v13, vcc
	s_and_b32 s11, s11, 0xffffe000
	v_add_u32_e32 v168, s11, v4
	v_add_u32_e32 v169, s11, v18
	v_add_co_u32_e32 v12, vcc, s26, v12
	v_lshl_add_u64 v[14:15], s[0:1], 0, v[8:9]
	s_nop 0
	v_addc_co_u32_e32 v13, vcc, 0, v13, vcc
	v_add_co_u32_e32 v14, vcc, s28, v14
	v_mov_b32_e32 v26, 0
	s_nop 0
	v_addc_co_u32_e32 v15, vcc, 0, v15, vcc
	v_mov_b32_e32 v27, 0
	v_mov_b32_e32 v28, 0
	v_mov_b32_e32 v29, 0
	v_mov_b32_e32 v30, 0
	v_mov_b32_e32 v31, 0
	v_mov_b32_e32 v32, 0
	v_mov_b32_e32 v33, 0
	s_add_i32 s29, s29, s2
	s_add_i32 s10, s10, s3
	v_lshl_add_u64 v[8:9], v[8:9], 0, s[6:7]
	v_lshl_add_u64 v[10:11], v[10:11], 0, s[8:9]
	s_cmpk_gt_i32 s29, 0x21ff
	s_waitcnt vmcnt(15)
	v_lshlrev_b32_e32 v90, 16, v66
	v_and_b32_e32 v91, 0xffff0000, v66
	s_waitcnt vmcnt(14)
	v_lshlrev_b32_e32 v92, 16, v68
	v_and_b32_e32 v93, 0xffff0000, v68
	s_waitcnt vmcnt(13)
	v_lshlrev_b32_e32 v94, 16, v70
	v_and_b32_e32 v95, 0xffff0000, v70
	s_waitcnt vmcnt(12)
	v_lshlrev_b32_e32 v96, 16, v72
	v_and_b32_e32 v97, 0xffff0000, v72
	s_waitcnt vmcnt(8)
	v_lshlrev_b32_e32 v84, 2, v84
	v_lshlrev_b32_e32 v85, 2, v85
	v_add_u32_e32 v84, s5, v84
	v_add_u32_e32 v85, s5, v85
	ds_read_b32 v84, v84
	ds_read_b32 v85, v85
	v_lshlrev_b32_e32 v66, 16, v67
	v_and_b32_e32 v67, 0xffff0000, v67
	v_lshlrev_b32_e32 v68, 16, v69
	s_waitcnt vmcnt(8) lgkmcnt(1)
	v_add_u32_e32 v84, v75, v84
	s_waitcnt vmcnt(8) lgkmcnt(0)
	v_add_u32_e32 v106, v87, v85
	v_ashrrev_i32_e32 v85, 31, v84
	v_ashrrev_i32_e32 v107, 31, v106
	v_lshlrev_b64 v[84:85], 12, v[84:85]
	v_lshlrev_b64 v[106:107], 12, v[106:107]
	v_lshl_add_u64 v[84:85], v[6:7], 0, v[84:85]
	v_lshl_add_u64 v[106:107], v[6:7], 0, v[106:107]
	global_load_dwordx2 v[108:109], v[84:85], off nt
	global_load_dwordx2 v[110:111], v[106:107], off nt
	global_load_dwordx2 v[112:113], v[84:85], off offset:512 nt
	global_load_dwordx2 v[114:115], v[106:107], off offset:512 nt
	global_load_dwordx2 v[116:117], v[84:85], off offset:1024 nt
	global_load_dwordx2 v[118:119], v[106:107], off offset:1024 nt
	global_load_dwordx2 v[120:121], v[84:85], off offset:1536 nt
	global_load_dwordx2 v[122:123], v[106:107], off offset:1536 nt
	global_load_dwordx2 v[124:125], v[84:85], off offset:2048 nt
	global_load_dwordx2 v[126:127], v[106:107], off offset:2048 nt
	global_load_dwordx2 v[128:129], v[84:85], off offset:2560 nt
	global_load_dwordx2 v[130:131], v[106:107], off offset:2560 nt
	global_load_dwordx2 v[132:133], v[84:85], off offset:3072 nt
	global_load_dwordx2 v[134:135], v[106:107], off offset:3072 nt
	s_nop 0
	global_load_dwordx2 v[84:85], v[84:85], off offset:3584 nt
	s_nop 0
	global_load_dwordx2 v[106:107], v[106:107], off offset:3584 nt
	v_and_b32_e32 v69, 0xffff0000, v69
	v_lshlrev_b32_e32 v70, 16, v71
	v_and_b32_e32 v71, 0xffff0000, v71
	v_lshlrev_b32_e32 v72, 16, v73
	v_and_b32_e32 v73, 0xffff0000, v73
	v_lshlrev_b32_e32 v98, 16, v76
	v_and_b32_e32 v99, 0xffff0000, v76
	v_lshlrev_b32_e32 v100, 16, v78
	v_and_b32_e32 v101, 0xffff0000, v78
	v_lshlrev_b32_e32 v76, 16, v77
	v_and_b32_e32 v77, 0xffff0000, v77
	v_lshlrev_b32_e32 v78, 16, v79
	v_and_b32_e32 v79, 0xffff0000, v79
	v_lshlrev_b32_e32 v102, 16, v80
	v_and_b32_e32 v103, 0xffff0000, v80
	v_lshlrev_b32_e32 v104, 16, v82
	v_and_b32_e32 v105, 0xffff0000, v82
	v_lshlrev_b32_e32 v82, 16, v83
	v_and_b32_e32 v83, 0xffff0000, v83
	v_lshlrev_b32_e32 v80, 16, v81
	v_and_b32_e32 v81, 0xffff0000, v81
	s_waitcnt vmcnt(15)
	v_lshlrev_b32_e32 v136, 16, v108
	s_waitcnt vmcnt(14)
	v_lshlrev_b32_e32 v138, 16, v110
	v_and_b32_e32 v139, 0xffff0000, v110
	v_lshlrev_b32_e32 v110, 16, v111
	v_and_b32_e32 v111, 0xffff0000, v111
	s_waitcnt vmcnt(12)
	v_lshlrev_b32_e32 v142, 16, v114
	v_and_b32_e32 v143, 0xffff0000, v114
	v_lshlrev_b32_e32 v114, 16, v115
	v_and_b32_e32 v115, 0xffff0000, v115
	s_waitcnt vmcnt(10)
	v_lshlrev_b32_e32 v146, 16, v118
	v_and_b32_e32 v147, 0xffff0000, v118
	v_lshlrev_b32_e32 v118, 16, v119
	v_and_b32_e32 v119, 0xffff0000, v119
	s_waitcnt vmcnt(8)
	v_lshlrev_b32_e32 v150, 16, v122
	v_and_b32_e32 v151, 0xffff0000, v122
	v_and_b32_e32 v137, 0xffff0000, v108
	v_lshlrev_b32_e32 v108, 16, v109
	v_and_b32_e32 v109, 0xffff0000, v109
	v_lshlrev_b32_e32 v140, 16, v112
	v_and_b32_e32 v141, 0xffff0000, v112
	v_lshlrev_b32_e32 v112, 16, v113
	v_and_b32_e32 v113, 0xffff0000, v113
	v_lshlrev_b32_e32 v144, 16, v116
	v_and_b32_e32 v145, 0xffff0000, v116
	v_lshlrev_b32_e32 v116, 16, v117
	v_and_b32_e32 v117, 0xffff0000, v117
	v_lshlrev_b32_e32 v148, 16, v120
	v_and_b32_e32 v149, 0xffff0000, v120
	v_lshlrev_b32_e32 v122, 16, v123
	v_and_b32_e32 v123, 0xffff0000, v123
	s_waitcnt vmcnt(6)
	v_lshlrev_b32_e32 v154, 16, v126
	v_and_b32_e32 v155, 0xffff0000, v126
	v_lshlrev_b32_e32 v126, 16, v127
	v_and_b32_e32 v127, 0xffff0000, v127
	s_waitcnt vmcnt(4)
	v_lshlrev_b32_e32 v158, 16, v130
	v_and_b32_e32 v159, 0xffff0000, v130
	v_lshlrev_b32_e32 v130, 16, v131
	v_and_b32_e32 v131, 0xffff0000, v131
	s_waitcnt vmcnt(2)
	v_lshlrev_b32_e32 v162, 16, v134
	v_and_b32_e32 v163, 0xffff0000, v134
	v_lshlrev_b32_e32 v134, 16, v135
	v_and_b32_e32 v135, 0xffff0000, v135
	s_waitcnt vmcnt(0)
	v_lshlrev_b32_e32 v166, 16, v106
	v_and_b32_e32 v167, 0xffff0000, v106
	v_lshlrev_b32_e32 v106, 16, v107
	v_and_b32_e32 v107, 0xffff0000, v107
	v_pk_mul_f32 v[138:139], v[88:89], v[138:139] op_sel_hi:[0,1]
	v_pk_mul_f32 v[110:111], v[88:89], v[110:111] op_sel_hi:[0,1]
	v_pk_mul_f32 v[142:143], v[88:89], v[142:143] op_sel_hi:[0,1]
	v_pk_mul_f32 v[114:115], v[88:89], v[114:115] op_sel_hi:[0,1]
	v_pk_mul_f32 v[146:147], v[88:89], v[146:147] op_sel_hi:[0,1]
	v_pk_mul_f32 v[118:119], v[88:89], v[118:119] op_sel_hi:[0,1]
	v_pk_mul_f32 v[150:151], v[88:89], v[150:151] op_sel_hi:[0,1]
	v_lshlrev_b32_e32 v120, 16, v121
	v_and_b32_e32 v121, 0xffff0000, v121
	v_lshlrev_b32_e32 v152, 16, v124
	v_and_b32_e32 v153, 0xffff0000, v124
	v_lshlrev_b32_e32 v124, 16, v125
	v_and_b32_e32 v125, 0xffff0000, v125
	v_lshlrev_b32_e32 v156, 16, v128
	v_and_b32_e32 v157, 0xffff0000, v128
	v_lshlrev_b32_e32 v128, 16, v129
	v_and_b32_e32 v129, 0xffff0000, v129
	v_lshlrev_b32_e32 v160, 16, v132
	v_and_b32_e32 v161, 0xffff0000, v132
	v_lshlrev_b32_e32 v132, 16, v133
	v_and_b32_e32 v133, 0xffff0000, v133
	v_lshlrev_b32_e32 v164, 16, v84
	v_and_b32_e32 v165, 0xffff0000, v84
	v_lshlrev_b32_e32 v84, 16, v85
	v_and_b32_e32 v85, 0xffff0000, v85
	v_pk_mul_f32 v[122:123], v[88:89], v[122:123] op_sel_hi:[0,1]
	v_pk_mul_f32 v[154:155], v[88:89], v[154:155] op_sel_hi:[0,1]
	v_pk_mul_f32 v[126:127], v[88:89], v[126:127] op_sel_hi:[0,1]
	v_pk_mul_f32 v[158:159], v[88:89], v[158:159] op_sel_hi:[0,1]
	v_pk_mul_f32 v[130:131], v[88:89], v[130:131] op_sel_hi:[0,1]
	v_pk_mul_f32 v[162:163], v[88:89], v[162:163] op_sel_hi:[0,1]
	v_pk_mul_f32 v[134:135], v[88:89], v[134:135] op_sel_hi:[0,1]
	v_pk_mul_f32 v[166:167], v[88:89], v[166:167] op_sel_hi:[0,1]
	v_pk_mul_f32 v[88:89], v[88:89], v[106:107] op_sel_hi:[0,1]
	v_pk_fma_f32 v[106:107], v[86:87], v[136:137], v[138:139] op_sel_hi:[0,1,1]
	v_pk_fma_f32 v[108:109], v[86:87], v[108:109], v[110:111] op_sel_hi:[0,1,1]
	v_pk_fma_f32 v[110:111], v[86:87], v[140:141], v[142:143] op_sel_hi:[0,1,1]
	v_pk_fma_f32 v[112:113], v[86:87], v[112:113], v[114:115] op_sel_hi:[0,1,1]
	v_pk_fma_f32 v[114:115], v[86:87], v[144:145], v[146:147] op_sel_hi:[0,1,1]
	v_pk_fma_f32 v[116:117], v[86:87], v[116:117], v[118:119] op_sel_hi:[0,1,1]
	v_pk_fma_f32 v[118:119], v[86:87], v[148:149], v[150:151] op_sel_hi:[0,1,1]
	v_pk_fma_f32 v[120:121], v[86:87], v[120:121], v[122:123] op_sel_hi:[0,1,1]
	v_pk_fma_f32 v[122:123], v[86:87], v[152:153], v[154:155] op_sel_hi:[0,1,1]
	v_pk_fma_f32 v[124:125], v[86:87], v[124:125], v[126:127] op_sel_hi:[0,1,1]
	v_pk_fma_f32 v[126:127], v[86:87], v[156:157], v[158:159] op_sel_hi:[0,1,1]
	v_pk_fma_f32 v[128:129], v[86:87], v[128:129], v[130:131] op_sel_hi:[0,1,1]
	v_pk_fma_f32 v[130:131], v[86:87], v[160:161], v[162:163] op_sel_hi:[0,1,1]
	v_pk_fma_f32 v[132:133], v[86:87], v[132:133], v[134:135] op_sel_hi:[0,1,1]
	v_pk_fma_f32 v[134:135], v[86:87], v[164:165], v[166:167] op_sel_hi:[0,1,1]
	v_pk_fma_f32 v[84:85], v[86:87], v[84:85], v[88:89] op_sel_hi:[0,1,1]
	v_pk_fma_f32 v[86:87], v[34:35], v[106:107], v[90:91]
	v_pk_fma_f32 v[88:89], v[38:39], v[110:111], v[92:93]
	v_pk_fma_f32 v[42:43], v[42:43], v[114:115], v[94:95]
	v_pk_fma_f32 v[46:47], v[46:47], v[118:119], v[96:97]
	v_mul_f32_e32 v75, v87, v87
	v_mul_f32_e32 v94, v89, v89
	v_mov_b32_e32 v38, v43
	v_mov_b32_e32 v39, v47
	v_pk_fma_f32 v[66:67], v[36:37], v[108:109], v[66:67]
	v_pk_fma_f32 v[68:69], v[40:41], v[112:113], v[68:69]
	v_pk_fma_f32 v[44:45], v[44:45], v[116:117], v[70:71]
	v_pk_fma_f32 v[48:49], v[48:49], v[120:121], v[72:73]
	v_pk_fma_f32 v[50:51], v[50:51], v[122:123], v[98:99]
	v_pk_fma_f32 v[54:55], v[54:55], v[126:127], v[100:101]
	v_cvt_pk_bf16_f32 v34, v86, v87
	v_cvt_pk_bf16_f32 v35, v66, v67
	v_mov_b32_e32 v36, v42
	v_mov_b32_e32 v37, v46
	v_fmac_f32_e32 v75, v86, v86
	v_fmac_f32_e32 v94, v88, v88
	v_pk_mul_f32 v[38:39], v[38:39], v[38:39]
	v_pk_fma_f32 v[52:53], v[52:53], v[124:125], v[76:77]
	v_mov_b32_e32 v40, v44
	v_mov_b32_e32 v41, v48
	v_mov_b32_e32 v76, v51
	v_mov_b32_e32 v77, v55
	global_store_dwordx2 v[16:17], v[34:35], off
	v_cvt_pk_bf16_f32 v34, v88, v89
	v_cvt_pk_bf16_f32 v35, v68, v69
	v_fmac_f32_e32 v75, v66, v66
	v_fmac_f32_e32 v94, v68, v68
	v_pk_fma_f32 v[36:37], v[36:37], v[36:37], v[38:39]
	v_pk_fma_f32 v[56:57], v[56:57], v[128:129], v[78:79]
	v_pk_fma_f32 v[58:59], v[58:59], v[130:131], v[102:103]
	v_pk_fma_f32 v[62:63], v[62:63], v[134:135], v[104:105]
	v_mov_b32_e32 v70, v45
	v_mov_b32_e32 v71, v49
	v_mov_b32_e32 v72, v50
	v_mov_b32_e32 v73, v54
	v_pk_mul_f32 v[76:77], v[76:77], v[76:77]
	global_store_dwordx2 v[16:17], v[34:35], off offset:512
	v_cvt_pk_bf16_f32 v34, v42, v43
	v_cvt_pk_bf16_f32 v35, v44, v45
	v_fmac_f32_e32 v75, v67, v67
	v_fmac_f32_e32 v94, v69, v69
	v_pk_fma_f32 v[36:37], v[40:41], v[40:41], v[36:37]
	v_pk_fma_f32 v[64:65], v[64:65], v[84:85], v[82:83]
	v_mov_b32_e32 v78, v52
	v_mov_b32_e32 v79, v56
	v_mov_b32_e32 v84, v59
	v_mov_b32_e32 v85, v63
	v_pk_fma_f32 v[38:39], v[72:73], v[72:73], v[76:77]
	global_store_dwordx2 v[16:17], v[34:35], off offset:1024
	v_cvt_pk_bf16_f32 v34, v46, v47
	v_cvt_pk_bf16_f32 v35, v48, v49
	v_add_f32_e32 v75, v75, v94
	v_pk_fma_f32 v[36:37], v[70:71], v[70:71], v[36:37]
	v_pk_fma_f32 v[60:61], v[60:61], v[132:133], v[80:81]
	v_mov_b32_e32 v80, v53
	v_mov_b32_e32 v81, v57
	v_mov_b32_e32 v82, v58
	v_mov_b32_e32 v83, v62
	v_pk_mul_f32 v[84:85], v[84:85], v[84:85]
	v_pk_fma_f32 v[38:39], v[78:79], v[78:79], v[38:39]
	global_store_dwordx2 v[16:17], v[34:35], off offset:1536
	v_cvt_pk_bf16_f32 v34, v50, v51
	v_cvt_pk_bf16_f32 v35, v52, v53
	v_add_f32_e32 v36, v75, v36
	v_mov_b32_e32 v90, v60
	v_mov_b32_e32 v91, v64
	v_pk_fma_f32 v[72:73], v[82:83], v[82:83], v[84:85]
	v_pk_fma_f32 v[70:71], v[80:81], v[80:81], v[38:39]
	global_store_dwordx2 v[16:17], v[34:35], off offset:2048
	v_cvt_pk_bf16_f32 v34, v54, v55
	v_cvt_pk_bf16_f32 v35, v56, v57
	v_add_f32_e32 v36, v36, v37
	v_mov_b32_e32 v92, v61
	v_mov_b32_e32 v93, v65
	v_pk_fma_f32 v[40:41], v[90:91], v[90:91], v[72:73]
	global_store_dwordx2 v[16:17], v[34:35], off offset:2560
	v_cvt_pk_bf16_f32 v34, v58, v59
	v_cvt_pk_bf16_f32 v35, v60, v61
	v_add_f32_e32 v70, v36, v70
	v_pk_fma_f32 v[72:73], v[92:93], v[92:93], v[40:41]
	global_store_dwordx2 v[16:17], v[34:35], off offset:3072
	v_cvt_pk_bf16_f32 v76, v62, v63
	v_cvt_pk_bf16_f32 v77, v64, v65
	ds_read_b128 v[34:37], v168
	ds_read_b128 v[38:41], v169
	global_store_dwordx2 v[16:17], v[76:77], off offset:3584
	v_add_f32_e32 v16, v70, v71
	v_add_f32_e32 v16, v16, v72
	v_add_f32_e32 v16, v16, v73
	v_mov_b32_e32 v17, v16
	s_nop 1
	v_mov_b32_dpp v17, v17 quad_perm:[1,0,3,2] row_mask:0xf bank_mask:0xf
	v_add_f32_e32 v16, v16, v17
	v_mov_b32_e32 v17, v16
	s_nop 1
	v_mov_b32_dpp v17, v17 quad_perm:[2,3,0,1] row_mask:0xf bank_mask:0xf
	v_add_f32_e32 v16, v16, v17
	v_mov_b32_e32 v17, v16
	s_nop 1
	v_mov_b32_dpp v17, v17 row_half_mirror row_mask:0xf bank_mask:0xf
	v_add_f32_e32 v16, v16, v17
	v_mov_b32_e32 v17, v16
	s_nop 1
	v_mov_b32_dpp v17, v17 row_mirror row_mask:0xf bank_mask:0xf
	v_add_f32_e32 v16, v16, v17
	s_nop 0
	v_readlane_b32 s11, v16, 16
	v_readlane_b32 s38, v16, 48
	v_readlane_b32 s30, v16, 0
	v_readlane_b32 s31, v16, 32
	v_mov_b32_e32 v16, s11
	v_mov_b32_e32 v17, s38
	v_pk_add_f32 v[16:17], s[30:31], v[16:17]
	s_nop 0
	v_add_f32_e32 v16, v16, v17
	v_fmamk_f32 v16, v16, 0x3a000000, v24
	v_mul_f32_e32 v17, 0x4b800000, v16
	v_cmp_gt_f32_e32 vcc, s25, v16
	s_nop 1
	v_cndmask_b32_e32 v16, v16, v17, vcc
	v_rsq_f32_e32 v16, v16
	s_nop 0
	v_mul_f32_e32 v17, 0x45800000, v16
	v_cndmask_b32_e32 v16, v16, v17, vcc
	v_mul_f32_e32 v17, v86, v16
	v_mul_f32_e32 v70, v87, v16
	v_mul_f32_e32 v66, v66, v16
	v_mul_f32_e32 v67, v67, v16
	s_waitcnt lgkmcnt(0)
	v_fma_f32 v34, v34, v17, v38
	v_fma_f32 v35, v35, v70, v39
	v_fma_f32 v36, v36, v66, v40
	v_fmac_f32_e32 v41, v37, v67
	v_mul_f32_e32 v71, v88, v16
	v_mul_f32_e32 v72, v89, v16
	v_mul_f32_e32 v68, v68, v16
	v_mul_f32_e32 v69, v69, v16
	v_mul_f32_e32 v42, v42, v16
	v_mul_f32_e32 v43, v43, v16
	v_mul_f32_e32 v44, v44, v16
	v_mul_f32_e32 v45, v45, v16
	v_mul_f32_e32 v46, v46, v16
	v_mul_f32_e32 v47, v47, v16
	v_mul_f32_e32 v48, v48, v16
	v_mul_f32_e32 v49, v49, v16
	v_mul_f32_e32 v50, v50, v16
	v_mul_f32_e32 v51, v51, v16
	v_mul_f32_e32 v52, v52, v16
	v_mul_f32_e32 v53, v53, v16
	v_mul_f32_e32 v54, v54, v16
	v_mul_f32_e32 v55, v55, v16
	v_mul_f32_e32 v56, v56, v16
	v_mul_f32_e32 v57, v57, v16
	v_mul_f32_e32 v58, v58, v16
	v_mul_f32_e32 v59, v59, v16
	v_mul_f32_e32 v60, v60, v16
	v_mul_f32_e32 v61, v61, v16
	v_mul_f32_e32 v62, v62, v16
	v_mul_f32_e32 v63, v63, v16
	v_mul_f32_e32 v64, v64, v16
	v_mul_f32_e32 v65, v65, v16
	v_cvt_pk_bf16_f32 v16, v34, v35
	v_cvt_pk_bf16_f32 v17, v36, v41
	v_med3_f32 v66, v34, s27, v25
	v_med3_f32 v67, v35, s27, v25
	v_med3_f32 v70, v36, s27, v25
	v_med3_f32 v73, v41, s27, v25
	ds_read_b128 v[34:37], v168 offset:1024
	ds_read_b128 v[38:41], v169 offset:1024
	v_cvt_pk_fp8_f32 v26, v66, v67
	global_store_dwordx2 v[12:13], v[16:17], off
	v_cvt_pk_fp8_f32 v26, v70, v73 op_sel:[0,0,1]
	s_waitcnt lgkmcnt(0)
	v_fma_f32 v16, v34, v71, v38
	v_fma_f32 v17, v35, v72, v39
	v_fma_f32 v34, v36, v68, v40
	v_med3_f32 v35, v16, s27, v25
	v_med3_f32 v36, v17, s27, v25
	v_cvt_pk_fp8_f32 v27, v35, v36
	v_fmac_f32_e32 v41, v37, v69
	v_med3_f32 v66, v34, s27, v25
	v_med3_f32 v67, v41, s27, v25
	global_store_dword v[14:15], v26, off
	v_cvt_pk_bf16_f32 v16, v16, v17
	v_cvt_pk_bf16_f32 v17, v34, v41
	ds_read_b128 v[34:37], v168 offset:2048
	ds_read_b128 v[38:41], v169 offset:2048
	v_cvt_pk_fp8_f32 v27, v66, v67 op_sel:[0,0,1]
	global_store_dwordx2 v[12:13], v[16:17], off offset:512
	s_waitcnt lgkmcnt(0)
	v_fma_f32 v26, v42, v34, v38
	v_fma_f32 v34, v43, v35, v39
	v_fma_f32 v35, v44, v36, v40
	v_fmac_f32_e32 v41, v45, v37
	global_store_dword v[14:15], v27, off offset:256
	v_cvt_pk_bf16_f32 v16, v26, v34
	v_cvt_pk_bf16_f32 v17, v35, v41
	v_med3_f32 v26, v26, s27, v25
	v_med3_f32 v27, v34, s27, v25
	v_med3_f32 v42, v35, s27, v25
	v_med3_f32 v43, v41, s27, v25
	ds_read_b128 v[34:37], v168 offset:3072
	ds_read_b128 v[38:41], v169 offset:3072
	v_cvt_pk_fp8_f32 v28, v26, v27
	global_store_dwordx2 v[12:13], v[16:17], off offset:1024
	v_cvt_pk_fp8_f32 v28, v42, v43 op_sel:[0,0,1]
	s_waitcnt lgkmcnt(0)
	v_fma_f32 v16, v46, v34, v38
	v_fma_f32 v17, v47, v35, v39
	v_med3_f32 v27, v16, s27, v25
	v_med3_f32 v34, v17, s27, v25
	v_cvt_pk_fp8_f32 v29, v27, v34
	v_fmac_f32_e32 v41, v49, v37
	v_fma_f32 v26, v48, v36, v40
	v_med3_f32 v43, v41, s27, v25
	global_store_dword v[14:15], v28, off offset:512
	v_cvt_pk_bf16_f32 v16, v16, v17
	v_cvt_pk_bf16_f32 v17, v26, v41
	ds_read_b128 v[34:37], v168 offset:4096
	ds_read_b128 v[38:41], v169 offset:4096
	v_med3_f32 v42, v26, s27, v25
	v_cvt_pk_fp8_f32 v29, v42, v43 op_sel:[0,0,1]
	global_store_dwordx2 v[12:13], v[16:17], off offset:1536
	s_waitcnt lgkmcnt(0)
	v_fma_f32 v26, v50, v34, v38
	v_fma_f32 v27, v51, v35, v39
	v_fma_f32 v28, v52, v36, v40
	v_fmac_f32_e32 v41, v53, v37
	global_store_dword v[14:15], v29, off offset:768
	v_cvt_pk_bf16_f32 v16, v26, v27
	v_cvt_pk_bf16_f32 v17, v28, v41
	v_med3_f32 v38, v26, s27, v25
	v_med3_f32 v39, v27, s27, v25
	v_med3_f32 v40, v28, s27, v25
	ds_read_b128 v[26:29], v168 offset:5120
	ds_read_b128 v[34:37], v169 offset:5120
	v_cvt_pk_fp8_f32 v30, v38, v39
	v_med3_f32 v41, v41, s27, v25
	global_store_dwordx2 v[12:13], v[16:17], off offset:2048
	v_cvt_pk_fp8_f32 v30, v40, v41 op_sel:[0,0,1]
	s_waitcnt lgkmcnt(0)
	v_fma_f32 v16, v54, v26, v34
	v_fma_f32 v17, v55, v27, v35
	v_fma_f32 v26, v56, v28, v36
	v_med3_f32 v27, v16, s27, v25
	v_med3_f32 v28, v17, s27, v25
	v_cvt_pk_fp8_f32 v31, v27, v28
	v_fmac_f32_e32 v37, v57, v29
	v_med3_f32 v38, v26, s27, v25
	v_med3_f32 v39, v37, s27, v25
	global_store_dword v[14:15], v30, off offset:1024
	v_cvt_pk_bf16_f32 v16, v16, v17
	v_cvt_pk_bf16_f32 v17, v26, v37
	ds_read_b128 v[26:29], v168 offset:6144
	ds_read_b128 v[34:37], v169 offset:6144
	v_cvt_pk_fp8_f32 v31, v38, v39 op_sel:[0,0,1]
	global_store_dwordx2 v[12:13], v[16:17], off offset:2560
	s_waitcnt lgkmcnt(0)
	v_fma_f32 v26, v58, v26, v34
	v_fma_f32 v27, v59, v27, v35
	v_fma_f32 v28, v60, v28, v36
	v_fmac_f32_e32 v37, v61, v29
	global_store_dword v[14:15], v31, off offset:1280
	v_cvt_pk_bf16_f32 v16, v26, v27
	v_cvt_pk_bf16_f32 v17, v28, v37
	v_med3_f32 v30, v26, s27, v25
	v_med3_f32 v31, v27, s27, v25
	v_med3_f32 v38, v28, s27, v25
	v_med3_f32 v39, v37, s27, v25
	ds_read_b128 v[26:29], v168 offset:7168
	ds_read_b128 v[34:37], v169 offset:7168
	v_cvt_pk_fp8_f32 v32, v30, v31
	global_store_dwordx2 v[12:13], v[16:17], off offset:3072
	s_waitcnt lgkmcnt(0)
	v_fma_f32 v16, v62, v26, v34
	v_fma_f32 v17, v63, v27, v35
	v_fma_f32 v26, v64, v28, v36
	v_med3_f32 v27, v16, s27, v25
	v_med3_f32 v28, v17, s27, v25
	v_cvt_pk_fp8_f32 v33, v27, v28
	v_cvt_pk_fp8_f32 v32, v38, v39 op_sel:[0,0,1]
	v_fmac_f32_e32 v37, v65, v29
	v_med3_f32 v27, v26, s27, v25
	v_med3_f32 v28, v37, s27, v25
	v_cvt_pk_fp8_f32 v33, v27, v28 op_sel:[0,0,1]
	global_store_dword v[14:15], v32, off offset:1536
	v_cvt_pk_bf16_f32 v16, v16, v17
	v_cvt_pk_bf16_f32 v17, v26, v37
	global_store_dwordx2 v[12:13], v[16:17], off offset:3584
	global_store_dword v[14:15], v33, off offset:1792
	s_cbranch_scc0 .LBB0_1411

.LBB0_2680:
	s_or_b64 exec, exec, s[0:1]
	s_add_i32 s0, 0, 0x20500
	v_mov_b32_e32 v0, s0
	s_waitcnt lgkmcnt(0)
	s_barrier
	ds_read_b64 v[0:1], v0
	s_ashr_i32 s6, s2, 6
	s_lshl_b32 s0, s14, 3
	s_add_i32 s0, s0, s6
	s_cmpk_gt_i32 s0, 0x1fff
	s_waitcnt lgkmcnt(0)
	v_readfirstlane_b32 s3, v0
	v_readfirstlane_b32 s4, v1
	s_cbranch_scc1 .LBB0_2683
	s_lshl_b32 s2, s7, 3
	s_add_u32 s10, s8, 0x326b8000
	s_addc_u32 s11, s9, 0
	s_add_u32 s12, s8, 0x326c9000
	s_addc_u32 s13, s9, 0
	s_add_u32 s16, s8, 0x326da000
	v_lshlrev_b32_e32 v0, 2, v4
	s_addc_u32 s17, s9, 0
	v_and_b32_e32 v8, 0xfc, v0
	s_add_u32 s18, s8, 0x10000
	v_mov_b32_e32 v1, 0
	v_lshlrev_b32_e32 v0, 1, v8
	s_addc_u32 s19, s9, 0
	v_lshl_add_u64 v[2:3], s[8:9], 0, v[0:1]
	s_mov_b64 s[20:21], 0x43d1c000
	s_ashr_i32 s1, s0, 31
	v_lshl_add_u64 v[2:3], v[2:3], 0, s[20:21]
	s_lshl_b64 s[20:21], s[0:1], 13
	v_and_b32_e32 v6, 63, v4
	s_add_u32 s20, s3, s20
	v_lshlrev_b32_e32 v0, 4, v6
	s_addc_u32 s21, s4, s21
	v_lshl_add_u64 v[4:5], s[20:21], 0, v[0:1]
	s_mov_b64 s[4:5], 0x1c00
	s_ashr_i32 s3, s2, 31
	s_lshl_b32 s14, s14, 4
	s_lshl_b32 s6, s6, 1
	v_lshl_add_u64 v[4:5], v[4:5], 0, s[4:5]
	s_lshl_b64 s[4:5], s[2:3], 13
	s_add_i32 s6, s14, s6
	s_lshl_b32 s14, s7, 4
	s_lshl_b64 s[20:21], s[0:1], 12
	s_add_u32 s8, s8, s20
	v_lshlrev_b32_e32 v0, 3, v6
	s_addc_u32 s9, s9, s21
	v_or_b32_e32 v10, 0x400, v8
	v_or_b32_e32 v12, 0x500, v8
	v_or_b32_e32 v14, 0x600, v8
	v_or_b32_e32 v16, 0x700, v8
	v_lshl_add_u64 v[6:7], s[8:9], 0, v[0:1]
	s_mov_b64 s[8:9], 0x29eb8000
	v_lshl_add_u64 v[6:7], v[6:7], 0, s[8:9]
	s_lshl_b64 s[8:9], s[2:3], 12
	s_add_i32 s1, 0, 0x20040
	v_lshlrev_b32_e32 v0, 2, v8
	v_lshlrev_b32_e32 v19, 2, v10
	v_lshlrev_b32_e32 v20, 2, v12
	v_lshlrev_b32_e32 v21, 2, v14
	v_lshlrev_b32_e32 v22, 2, v16
	s_movk_i32 s3, 0xf000
	s_mov_b32 s24, s6
	s_ashr_i32 s25, s24, 31
	s_lshl_b64 s[20:21], s[24:25], 2
	s_add_u32 s22, s10, s20
	s_addc_u32 s23, s11, s21
	global_load_dwordx2 v[150:151], v1, s[22:23]
	s_add_u32 s22, s12, s20
	s_addc_u32 s23, s13, s21
	global_load_dword v152, v1, s[22:23]
	s_add_u32 s22, s16, s20
	s_addc_u32 s23, s17, s21
	global_load_dword v154, v1, s[22:23]
	s_add_i32 s24, s24, 1
	s_ashr_i32 s25, s24, 31
	s_lshl_b64 s[20:21], s[24:25], 2
	s_add_u32 s22, s12, s20
	s_addc_u32 s23, s13, s21
	global_load_dword v153, v1, s[22:23]
	s_add_u32 s22, s16, s20
	s_addc_u32 s23, s17, s21
	global_load_dword v155, v1, s[22:23]
	s_waitcnt vmcnt(0)
.LBB0_2682:
	v_mov_b32_e32 v64, v150
	v_mov_b32_e32 v65, v151
	v_mov_b32_e32 v23, v152
	v_mov_b32_e32 v67, v153
	v_mov_b32_e32 v66, v154
	v_mov_b32_e32 v68, v155
	s_add_i32 s24, s6, s14
	s_ashr_i32 s25, s24, 31
	s_lshl_b64 s[20:21], s[24:25], 2
	s_add_u32 s22, s10, s20
	s_addc_u32 s23, s11, s21
	global_load_dwordx2 v[150:151], v1, s[22:23]
	s_add_u32 s22, s12, s20
	s_addc_u32 s23, s13, s21
	global_load_dword v152, v1, s[22:23]
	s_add_u32 s22, s16, s20
	s_addc_u32 s23, s17, s21
	global_load_dword v154, v1, s[22:23]
	s_add_i32 s24, s24, 1
	s_ashr_i32 s25, s24, 31
	s_lshl_b64 s[20:21], s[24:25], 2
	s_add_u32 s22, s12, s20
	s_addc_u32 s23, s13, s21
	global_load_dword v153, v1, s[22:23]
	s_add_u32 s22, s16, s20
	s_addc_u32 s23, s17, s21
	global_load_dword v155, v1, s[22:23]
	global_load_dwordx2 v[8:9], v[6:7], off nt
	global_load_dwordx2 v[10:11], v[6:7], off offset:512 nt
	global_load_dwordx2 v[12:13], v[6:7], off offset:1024 nt
	global_load_dwordx2 v[14:15], v[6:7], off offset:1536 nt
	global_load_dwordx2 v[56:57], v[6:7], off offset:2048 nt
	global_load_dwordx2 v[58:59], v[6:7], off offset:2560 nt
	global_load_dwordx2 v[60:61], v[6:7], off offset:3072 nt
	global_load_dwordx2 v[62:63], v[6:7], off offset:3584 nt
	s_ashr_i32 s7, s0, 12
	s_mul_i32 s20, s7, 6
	s_ashr_i32 s21, s20, 31
	s_lshl_b64 s[20:21], s[20:21], 13
	s_add_u32 s7, s18, s20
	s_addc_u32 s21, s19, s21
	s_add_u32 s20, s7, 0x2e000
	s_addc_u32 s21, s21, 0
	global_load_dwordx4 v[24:27], v0, s[20:21]
	global_load_dwordx4 v[28:31], v0, s[20:21] offset:1024
	global_load_dwordx4 v[32:35], v0, s[20:21] offset:2048
	global_load_dwordx4 v[36:39], v0, s[20:21] offset:3072
	global_load_dwordx4 v[40:43], v19, s[20:21]
	global_load_dwordx4 v[44:47], v20, s[20:21]
	global_load_dwordx4 v[48:51], v21, s[20:21]
	global_load_dwordx4 v[52:55], v22, s[20:21]
	v_add_co_u32_e32 v16, vcc, s3, v4
	s_add_i32 s0, s0, s2
	s_nop 0
	v_addc_co_u32_e32 v17, vcc, -1, v5, vcc
	s_add_i32 s6, s6, s14
	v_lshl_add_u64 v[6:7], v[6:7], 0, s[8:9]
	s_cmpk_lt_i32 s0, 0x2000
	s_waitcnt vmcnt(15)
	v_lshlrev_b32_e32 v70, 16, v8
	s_waitcnt vmcnt(14)
	v_lshlrev_b32_e32 v72, 16, v10
	v_and_b32_e32 v73, 0xffff0000, v10
	v_lshlrev_b32_e32 v74, 16, v11
	v_and_b32_e32 v75, 0xffff0000, v11
	s_waitcnt vmcnt(13)
	v_lshlrev_b32_e32 v76, 16, v12
	v_and_b32_e32 v77, 0xffff0000, v12
	s_waitcnt vmcnt(8)
	v_lshlrev_b32_e32 v10, 2, v64
	v_lshlrev_b32_e32 v11, 2, v65
	v_add_u32_e32 v10, s1, v10
	v_add_u32_e32 v11, s1, v11
	ds_read_b32 v10, v10
	ds_read_b32 v11, v11
	v_lshlrev_b32_e32 v78, 16, v13
	v_and_b32_e32 v79, 0xffff0000, v13
	v_lshlrev_b32_e32 v80, 16, v14
	s_waitcnt vmcnt(8) lgkmcnt(1)
	v_add_u32_e32 v10, v23, v10
	s_waitcnt vmcnt(8) lgkmcnt(0)
	v_add_u32_e32 v12, v67, v11
	v_ashrrev_i32_e32 v11, 31, v10
	v_ashrrev_i32_e32 v13, 31, v12
	v_lshlrev_b64 v[10:11], 12, v[10:11]
	v_lshlrev_b64 v[12:13], 12, v[12:13]
	v_lshl_add_u64 v[10:11], v[2:3], 0, v[10:11]
	v_and_b32_e32 v81, 0xffff0000, v14
	v_lshlrev_b32_e32 v82, 16, v15
	v_and_b32_e32 v83, 0xffff0000, v15
	v_lshl_add_u64 v[12:13], v[2:3], 0, v[12:13]
	global_load_dwordx2 v[14:15], v[10:11], off nt
	global_load_dwordx2 v[64:65], v[12:13], off nt
	global_load_dwordx2 v[92:93], v[10:11], off offset:512 nt
	global_load_dwordx2 v[94:95], v[12:13], off offset:512 nt
	global_load_dwordx2 v[96:97], v[10:11], off offset:1024 nt
	global_load_dwordx2 v[98:99], v[12:13], off offset:1024 nt
	global_load_dwordx2 v[100:101], v[10:11], off offset:1536 nt
	global_load_dwordx2 v[102:103], v[12:13], off offset:1536 nt
	global_load_dwordx2 v[104:105], v[10:11], off offset:2048 nt
	global_load_dwordx2 v[106:107], v[12:13], off offset:2048 nt
	global_load_dwordx2 v[108:109], v[10:11], off offset:2560 nt
	global_load_dwordx2 v[110:111], v[12:13], off offset:2560 nt
	global_load_dwordx2 v[112:113], v[10:11], off offset:3072 nt
	global_load_dwordx2 v[114:115], v[12:13], off offset:3072 nt
	global_load_dwordx2 v[116:117], v[10:11], off offset:3584 nt
	s_nop 0
	global_load_dwordx2 v[10:11], v[12:13], off offset:3584 nt
	v_and_b32_e32 v71, 0xffff0000, v8
	v_lshlrev_b32_e32 v8, 16, v9
	v_and_b32_e32 v9, 0xffff0000, v9
	v_lshlrev_b32_e32 v84, 16, v56
	v_and_b32_e32 v85, 0xffff0000, v56
	v_lshlrev_b32_e32 v56, 16, v57
	v_and_b32_e32 v57, 0xffff0000, v57
	v_lshlrev_b32_e32 v86, 16, v58
	v_and_b32_e32 v87, 0xffff0000, v58
	v_lshlrev_b32_e32 v58, 16, v59
	v_and_b32_e32 v59, 0xffff0000, v59
	v_lshlrev_b32_e32 v88, 16, v60
	v_and_b32_e32 v89, 0xffff0000, v60
	v_lshlrev_b32_e32 v60, 16, v61
	v_and_b32_e32 v61, 0xffff0000, v61
	v_lshlrev_b32_e32 v90, 16, v62
	v_and_b32_e32 v91, 0xffff0000, v62
	v_lshlrev_b32_e32 v62, 16, v63
	v_and_b32_e32 v63, 0xffff0000, v63
	s_waitcnt vmcnt(15)
	v_lshlrev_b32_e32 v12, 16, v14
	s_waitcnt vmcnt(14)
	v_lshlrev_b32_e32 v118, 16, v64
	v_and_b32_e32 v119, 0xffff0000, v64
	v_lshlrev_b32_e32 v64, 16, v65
	v_and_b32_e32 v65, 0xffff0000, v65
	v_and_b32_e32 v13, 0xffff0000, v14
	v_lshlrev_b32_e32 v14, 16, v15
	v_and_b32_e32 v15, 0xffff0000, v15
	s_waitcnt vmcnt(12)
	v_lshlrev_b32_e32 v122, 16, v94
	v_and_b32_e32 v123, 0xffff0000, v94
	v_lshlrev_b32_e32 v94, 16, v95
	v_and_b32_e32 v95, 0xffff0000, v95
	s_waitcnt vmcnt(10)
	v_lshlrev_b32_e32 v126, 16, v98
	v_and_b32_e32 v127, 0xffff0000, v98
	v_lshlrev_b32_e32 v98, 16, v99
	v_and_b32_e32 v99, 0xffff0000, v99
	s_waitcnt vmcnt(8)
	v_lshlrev_b32_e32 v130, 16, v102
	v_and_b32_e32 v131, 0xffff0000, v102
	v_lshlrev_b32_e32 v102, 16, v103
	v_and_b32_e32 v103, 0xffff0000, v103
	s_waitcnt vmcnt(6)
	v_lshlrev_b32_e32 v134, 16, v106
	v_and_b32_e32 v135, 0xffff0000, v106
	v_lshlrev_b32_e32 v106, 16, v107
	v_and_b32_e32 v107, 0xffff0000, v107
	s_waitcnt vmcnt(4)
	v_lshlrev_b32_e32 v138, 16, v110
	v_and_b32_e32 v139, 0xffff0000, v110
	v_lshlrev_b32_e32 v110, 16, v111
	v_and_b32_e32 v111, 0xffff0000, v111
	s_waitcnt vmcnt(2)
	v_lshlrev_b32_e32 v142, 16, v114
	v_and_b32_e32 v143, 0xffff0000, v114
	v_lshlrev_b32_e32 v114, 16, v115
	v_and_b32_e32 v115, 0xffff0000, v115
	s_waitcnt vmcnt(0)
	v_lshlrev_b32_e32 v146, 16, v10
	v_and_b32_e32 v147, 0xffff0000, v10
	v_lshlrev_b32_e32 v10, 16, v11
	v_and_b32_e32 v11, 0xffff0000, v11
	v_pk_mul_f32 v[118:119], v[68:69], v[118:119] op_sel_hi:[0,1]
	v_pk_mul_f32 v[64:65], v[68:69], v[64:65] op_sel_hi:[0,1]
	v_lshlrev_b32_e32 v120, 16, v92
	v_and_b32_e32 v121, 0xffff0000, v92
	v_lshlrev_b32_e32 v92, 16, v93
	v_and_b32_e32 v93, 0xffff0000, v93
	v_lshlrev_b32_e32 v124, 16, v96
	v_and_b32_e32 v125, 0xffff0000, v96
	v_lshlrev_b32_e32 v96, 16, v97
	v_and_b32_e32 v97, 0xffff0000, v97
	v_lshlrev_b32_e32 v128, 16, v100
	v_and_b32_e32 v129, 0xffff0000, v100
	v_lshlrev_b32_e32 v100, 16, v101
	v_and_b32_e32 v101, 0xffff0000, v101
	v_lshlrev_b32_e32 v132, 16, v104
	v_and_b32_e32 v133, 0xffff0000, v104
	v_lshlrev_b32_e32 v104, 16, v105
	v_and_b32_e32 v105, 0xffff0000, v105
	v_lshlrev_b32_e32 v136, 16, v108
	v_and_b32_e32 v137, 0xffff0000, v108
	v_lshlrev_b32_e32 v108, 16, v109
	v_and_b32_e32 v109, 0xffff0000, v109
	v_lshlrev_b32_e32 v140, 16, v112
	v_and_b32_e32 v141, 0xffff0000, v112
	v_lshlrev_b32_e32 v112, 16, v113
	v_and_b32_e32 v113, 0xffff0000, v113
	v_lshlrev_b32_e32 v144, 16, v116
	v_and_b32_e32 v145, 0xffff0000, v116
	v_lshlrev_b32_e32 v116, 16, v117
	v_and_b32_e32 v117, 0xffff0000, v117
	v_pk_mul_f32 v[122:123], v[68:69], v[122:123] op_sel_hi:[0,1]
	v_pk_mul_f32 v[94:95], v[68:69], v[94:95] op_sel_hi:[0,1]
	v_pk_mul_f32 v[126:127], v[68:69], v[126:127] op_sel_hi:[0,1]
	v_pk_mul_f32 v[98:99], v[68:69], v[98:99] op_sel_hi:[0,1]
	v_pk_mul_f32 v[130:131], v[68:69], v[130:131] op_sel_hi:[0,1]
	v_pk_mul_f32 v[102:103], v[68:69], v[102:103] op_sel_hi:[0,1]
	v_pk_mul_f32 v[134:135], v[68:69], v[134:135] op_sel_hi:[0,1]
	v_pk_mul_f32 v[106:107], v[68:69], v[106:107] op_sel_hi:[0,1]
	v_pk_mul_f32 v[138:139], v[68:69], v[138:139] op_sel_hi:[0,1]
	v_pk_mul_f32 v[110:111], v[68:69], v[110:111] op_sel_hi:[0,1]
	v_pk_mul_f32 v[142:143], v[68:69], v[142:143] op_sel_hi:[0,1]
	v_pk_mul_f32 v[114:115], v[68:69], v[114:115] op_sel_hi:[0,1]
	v_pk_mul_f32 v[146:147], v[68:69], v[146:147] op_sel_hi:[0,1]
	v_pk_mul_f32 v[10:11], v[68:69], v[10:11] op_sel_hi:[0,1]
	v_pk_fma_f32 v[12:13], v[66:67], v[12:13], v[118:119] op_sel_hi:[0,1,1]
	v_pk_fma_f32 v[14:15], v[66:67], v[14:15], v[64:65] op_sel_hi:[0,1,1]
	v_pk_fma_f32 v[64:65], v[66:67], v[120:121], v[122:123] op_sel_hi:[0,1,1]
	v_pk_fma_f32 v[68:69], v[66:67], v[92:93], v[94:95] op_sel_hi:[0,1,1]
	v_pk_fma_f32 v[92:93], v[66:67], v[124:125], v[126:127] op_sel_hi:[0,1,1]
	v_pk_fma_f32 v[94:95], v[66:67], v[96:97], v[98:99] op_sel_hi:[0,1,1]
	v_pk_fma_f32 v[96:97], v[66:67], v[128:129], v[130:131] op_sel_hi:[0,1,1]
	v_pk_fma_f32 v[98:99], v[66:67], v[100:101], v[102:103] op_sel_hi:[0,1,1]
	v_pk_fma_f32 v[100:101], v[66:67], v[132:133], v[134:135] op_sel_hi:[0,1,1]
	v_pk_fma_f32 v[102:103], v[66:67], v[104:105], v[106:107] op_sel_hi:[0,1,1]
	v_pk_fma_f32 v[104:105], v[66:67], v[136:137], v[138:139] op_sel_hi:[0,1,1]
	v_pk_fma_f32 v[106:107], v[66:67], v[108:109], v[110:111] op_sel_hi:[0,1,1]
	v_pk_fma_f32 v[108:109], v[66:67], v[140:141], v[142:143] op_sel_hi:[0,1,1]
	v_pk_fma_f32 v[110:111], v[66:67], v[112:113], v[114:115] op_sel_hi:[0,1,1]
	v_pk_fma_f32 v[112:113], v[66:67], v[144:145], v[146:147] op_sel_hi:[0,1,1]
	v_pk_fma_f32 v[66:67], v[66:67], v[116:117], v[10:11] op_sel_hi:[0,1,1]
	v_pk_fma_f32 v[10:11], v[26:27], v[14:15], v[8:9]
	v_pk_fma_f32 v[8:9], v[24:25], v[12:13], v[70:71]
	v_pk_fma_f32 v[14:15], v[30:31], v[68:69], v[74:75]
	v_pk_fma_f32 v[12:13], v[28:29], v[64:65], v[72:73]
	v_pk_fma_f32 v[26:27], v[34:35], v[94:95], v[78:79]
	v_pk_fma_f32 v[24:25], v[32:33], v[92:93], v[76:77]
	v_pk_fma_f32 v[30:31], v[38:39], v[98:99], v[82:83]
	v_pk_fma_f32 v[28:29], v[36:37], v[96:97], v[80:81]
	v_pk_fma_f32 v[34:35], v[42:43], v[102:103], v[56:57]
	v_pk_fma_f32 v[32:33], v[40:41], v[100:101], v[84:85]
	v_pk_fma_f32 v[38:39], v[46:47], v[106:107], v[58:59]
	v_pk_fma_f32 v[36:37], v[44:45], v[104:105], v[86:87]
	v_pk_fma_f32 v[42:43], v[50:51], v[110:111], v[60:61]
	v_pk_fma_f32 v[40:41], v[48:49], v[108:109], v[88:89]
	v_pk_fma_f32 v[46:47], v[54:55], v[66:67], v[62:63]
	v_pk_fma_f32 v[44:45], v[52:53], v[112:113], v[90:91]
	global_store_dwordx4 v[16:17], v[8:11], off offset:-3072 nt
	global_store_dwordx4 v[16:17], v[12:15], off offset:-2048 nt
	global_store_dwordx4 v[16:17], v[24:27], off offset:-1024 nt
	global_store_dwordx4 v[4:5], v[28:31], off offset:-4096 nt
	global_store_dwordx4 v[4:5], v[32:35], off offset:-3072 nt
	global_store_dwordx4 v[4:5], v[36:39], off offset:-2048 nt
	global_store_dwordx4 v[4:5], v[40:43], off offset:-1024 nt
	global_store_dwordx4 v[4:5], v[44:47], off nt
	v_lshl_add_u64 v[4:5], v[4:5], 0, s[4:5]
	s_cbranch_scc1 .LBB0_2682
